# attention loop: each half-iteration opens with its first QK MFMA (operands resident) ahead of the scalar index math and K-fragment ds_reads
# speedup vs baseline: 1.0163x; 1.0163x over previous
.LBB0_1319:
	v_mfma_f32_32x32x16_bf16 v[82:97], v[138:141], v[98:101], 0
	s_add_i32 s45, s44, -2
	s_mul_hi_i32 s50, s45, 0x55555556
	s_mul_i32 s50, s50, 3
	s_sub_i32 s45, s45, s50
	v_lshl_add_u32 v162, s45, 13, v240
	ds_read_b64_tr_b16 v[142:143], v162 offset:40960
	ds_read_b64_tr_b16 v[144:145], v162 offset:41472
	s_add_i32 s45, s44, -1
	v_add_f32_e32 v66, v50, v51
	v_add_f32_e32 v67, v52, v53
	v_add_f32_e32 v66, v66, v67
	v_cvt_pk_bf16_f32 v138, v50, v51
	v_cvt_pk_bf16_f32 v139, v52, v53
	ds_read_b64_tr_b16 v[146:147], v162 offset:45056
	ds_read_b64_tr_b16 v[148:149], v162 offset:45568
	v_add_f32_e32 v50, v54, v55
	v_add_f32_e32 v51, v56, v57
	v_add_f32_e32 v50, v50, v51
	v_add_f32_e32 v50, v50, v66
	v_mfma_f32_32x32x16_bf16 v[66:81], v[130:133], v[98:101], 0
	v_cvt_pk_bf16_f32 v140, v54, v55
	v_cvt_pk_bf16_f32 v141, v56, v57
	s_and_b32 s50, s45, 3
	s_mulk_i32 s50, 0x2800
	v_add_u32_e32 v150, s50, v238
	ds_read_b128 v[130:133], v150 offset:6144
	ds_read_b128 v[158:161], v150 offset:6656
	ds_read_b64_tr_b16 v[54:55], v162 offset:41984
	ds_read_b64_tr_b16 v[56:57], v162 offset:42496
	v_mfma_f32_32x32x16_bf16 v[82:97], v[134:137], v[102:105], v[82:97]
	v_add_f32_e32 v51, v58, v59
	v_add_f32_e32 v52, v60, v61
	v_add_f32_e32 v51, v51, v52
	v_add_f32_e32 v52, v51, v50
	v_cvt_pk_bf16_f32 v50, v58, v59
	v_cvt_pk_bf16_f32 v51, v60, v61
	ds_read_b64_tr_b16 v[58:59], v162 offset:46080
	ds_read_b64_tr_b16 v[60:61], v162 offset:46592
	v_mfma_f32_32x32x16_bf16 v[66:81], v[126:129], v[102:105], v[66:81]
	v_add_f32_e32 v53, v62, v63
	v_add_f32_e32 v126, v64, v65
	v_add_f32_e32 v53, v53, v126
	v_add_f32_e32 v151, v53, v52
	v_cvt_pk_bf16_f32 v52, v62, v63
	v_cvt_pk_bf16_f32 v53, v64, v65
	ds_read_b128 v[126:129], v150 offset:8192
	ds_read_b128 v[134:137], v150 offset:8704
	ds_read_b64_tr_b16 v[62:63], v162 offset:43008
	ds_read_b64_tr_b16 v[64:65], v162 offset:43520
	v_mfma_f32_32x32x16_bf16 v[82:97], v[122:125], v[106:109], v[82:97]
	v_add_f32_e32 v122, v34, v35
	v_add_f32_e32 v123, v36, v37
	v_add_f32_e32 v122, v122, v123
	v_add_f32_e32 v122, v122, v151
	v_cvt_pk_bf16_f32 v34, v34, v35
	v_cvt_pk_bf16_f32 v35, v36, v37
	ds_read_b64_tr_b16 v[150:151], v162 offset:47104
	ds_read_b64_tr_b16 v[152:153], v162 offset:47616
	v_mfma_f32_32x32x16_bf16 v[66:81], v[118:121], v[106:109], v[66:81]
	v_add_f32_e32 v36, v38, v39
	v_add_f32_e32 v37, v40, v41
	v_add_f32_e32 v36, v36, v37
	v_add_f32_e32 v118, v36, v122
	v_cvt_pk_bf16_f32 v36, v38, v39
	v_cvt_pk_bf16_f32 v37, v40, v41
	ds_read_b64_tr_b16 v[154:155], v162 offset:44032
	ds_read_b64_tr_b16 v[156:157], v162 offset:44544
	s_waitcnt lgkmcnt(13)
	v_mfma_f32_32x32x16_bf16 v[82:97], v[130:133], v[110:113], v[82:97]
	v_add_f32_e32 v38, v42, v43
	v_add_f32_e32 v39, v44, v45
	v_add_f32_e32 v38, v38, v39
	v_add_f32_e32 v40, v38, v118
	v_cvt_pk_bf16_f32 v38, v42, v43
	v_cvt_pk_bf16_f32 v39, v44, v45
	ds_read_b64_tr_b16 v[42:43], v162 offset:48128
	ds_read_b64_tr_b16 v[44:45], v162 offset:48640
	s_waitcnt lgkmcnt(14)
	v_mfma_f32_32x32x16_bf16 v[66:81], v[158:161], v[110:113], v[66:81]
	v_add_f32_e32 v41, v46, v47
	v_add_f32_e32 v118, v48, v49
	v_add_f32_e32 v41, v41, v118
	v_add_f32_e32 v166, v41, v40
	v_cvt_pk_bf16_f32 v40, v46, v47
	v_cvt_pk_bf16_f32 v41, v48, v49
	s_waitcnt lgkmcnt(9)
	v_mfma_f32_32x32x16_bf16 v[82:97], v[126:129], v[114:117], v[82:97]
	s_waitcnt lgkmcnt(8)
	v_mfma_f32_32x32x16_bf16 v[66:81], v[134:137], v[114:117], v[66:81]
	s_add_i32 s61, s44, 2
	s_cmp_lt_i32 s61, s71
	s_cselect_b64 s[52:53], -1, 0
	s_cmp_ge_i32 s61, s71
	s_cselect_b64 s[50:51], -1, 0
	s_cbranch_scc1 .LBB0_1322
	s_and_b32 s54, s61, 3
	s_mulk_i32 s54, 0x2800
	s_add_i32 s55, s54, s66
	s_mov_b32 m0, s55
	s_nop 0
	global_load_lds_dwordx4 v[222:223], off
	s_and_b64 vcc, exec, s[42:43]
	s_cbranch_vccnz .LBB0_1322
	s_add_i32 s54, s54, s70
	s_mov_b32 m0, s54
	s_nop 0
	global_load_lds_dwordx4 v[220:221], off

.LBB0_1331:
	v_mfma_f32_32x32x16_bf16 v[50:65], v[138:141], v[98:101], 0
	s_mul_hi_i32 s52, s45, 0x55555556
	s_mul_i32 s52, s52, 3
	s_sub_i32 s45, s45, s52
	v_lshl_add_u32 v199, s45, 13, v240
	ds_read_b64_tr_b16 v[162:163], v199 offset:40960
	ds_read_b64_tr_b16 v[164:165], v199 offset:41472
	s_waitcnt lgkmcnt(7)
	v_add_f32_e32 v34, v82, v83
	v_add_f32_e32 v35, v84, v85
	v_add_f32_e32 v34, v34, v35
	v_cvt_pk_bf16_f32 v154, v82, v83
	v_cvt_pk_bf16_f32 v155, v84, v85
	ds_read_b64_tr_b16 v[158:159], v199 offset:45056
	ds_read_b64_tr_b16 v[160:161], v199 offset:45568
	v_add_f32_e32 v35, v86, v87
	v_add_f32_e32 v36, v88, v89
	v_add_f32_e32 v35, v35, v36
	v_add_f32_e32 v82, v35, v34
	s_waitcnt lgkmcnt(8)
	v_mfma_f32_32x32x16_bf16 v[34:49], v[130:133], v[98:101], 0
	v_cvt_pk_bf16_f32 v156, v86, v87
	v_cvt_pk_bf16_f32 v157, v88, v89
	ds_read_b128 v[170:173], v197 offset:6144
	ds_read_b128 v[174:177], v197 offset:6656
	ds_read_b64_tr_b16 v[150:151], v199 offset:41984
	ds_read_b64_tr_b16 v[152:153], v199 offset:42496
	s_waitcnt lgkmcnt(11)
	v_mfma_f32_32x32x16_bf16 v[50:65], v[134:137], v[102:105], v[50:65]
	v_add_f32_e32 v83, v90, v91
	v_add_f32_e32 v84, v92, v93
	v_add_f32_e32 v83, v83, v84
	v_add_f32_e32 v82, v83, v82
	v_cvt_pk_bf16_f32 v142, v90, v91
	v_cvt_pk_bf16_f32 v143, v92, v93
	ds_read_b64_tr_b16 v[146:147], v199 offset:46080
	ds_read_b64_tr_b16 v[148:149], v199 offset:46592
	s_waitcnt lgkmcnt(12)
	v_mfma_f32_32x32x16_bf16 v[34:49], v[126:129], v[102:105], v[34:49]
	v_add_f32_e32 v83, v94, v95
	v_add_f32_e32 v84, v96, v97
	v_add_f32_e32 v83, v83, v84
	v_add_f32_e32 v82, v83, v82
	v_cvt_pk_bf16_f32 v144, v94, v95
	v_cvt_pk_bf16_f32 v145, v96, v97
	ds_read_b128 v[248:251], v197 offset:8192
	ds_read_b128 v[232:235], v197 offset:8704
	ds_read_b64_tr_b16 v[90:91], v199 offset:43008
	ds_read_b64_tr_b16 v[92:93], v199 offset:43520
	s_waitcnt lgkmcnt(14)
	v_mfma_f32_32x32x16_bf16 v[50:65], v[122:125], v[106:109], v[50:65]
	v_add_f32_e32 v83, v66, v67
	v_add_f32_e32 v84, v68, v69
	v_add_f32_e32 v83, v83, v84
	v_add_f32_e32 v84, v83, v82
	v_cvt_pk_bf16_f32 v82, v66, v67
	v_cvt_pk_bf16_f32 v83, v68, v69
	ds_read_b64_tr_b16 v[86:87], v199 offset:47104
	ds_read_b64_tr_b16 v[88:89], v199 offset:47616
	v_mfma_f32_32x32x16_bf16 v[34:49], v[118:121], v[106:109], v[34:49]
	v_add_f32_e32 v66, v70, v71
	v_add_f32_e32 v67, v72, v73
	v_add_f32_e32 v66, v66, v67
	v_add_f32_e32 v66, v66, v84
	v_cvt_pk_bf16_f32 v84, v70, v71
	v_cvt_pk_bf16_f32 v85, v72, v73
	ds_read_b64_tr_b16 v[70:71], v199 offset:44032
	ds_read_b64_tr_b16 v[72:73], v199 offset:44544
	s_waitcnt lgkmcnt(13)
	v_mfma_f32_32x32x16_bf16 v[50:65], v[170:173], v[110:113], v[50:65]
	v_add_f32_e32 v67, v74, v75
	v_add_f32_e32 v68, v76, v77
	v_add_f32_e32 v67, v67, v68
	v_add_f32_e32 v68, v67, v66
	v_cvt_pk_bf16_f32 v66, v74, v75
	v_cvt_pk_bf16_f32 v67, v76, v77
	ds_read_b64_tr_b16 v[74:75], v199 offset:48128
	ds_read_b64_tr_b16 v[76:77], v199 offset:48640
	s_waitcnt lgkmcnt(14)
	v_mfma_f32_32x32x16_bf16 v[34:49], v[174:177], v[110:113], v[34:49]
	v_add_f32_e32 v69, v78, v79
	v_add_f32_e32 v94, v80, v81
	v_add_f32_e32 v69, v69, v94
	v_add_f32_e32 v94, v69, v68
	v_cvt_pk_bf16_f32 v68, v78, v79
	v_cvt_pk_bf16_f32 v69, v80, v81
	s_waitcnt lgkmcnt(9)
	v_mfma_f32_32x32x16_bf16 v[50:65], v[248:251], v[114:117], v[50:65]
	s_waitcnt lgkmcnt(8)
	v_mfma_f32_32x32x16_bf16 v[34:49], v[232:235], v[114:117], v[34:49]
	s_add_i32 s54, s44, 3
	s_cmp_lt_i32 s54, s71
	s_cselect_b64 s[52:53], -1, 0
	s_cbranch_scc0 .LBB0_1334
	s_ashr_i32 s55, s54, 31
	s_and_b32 s45, s54, 3
	s_lshl_b64 s[58:59], s[54:55], 17
	s_mulk_i32 s45, 0x2800
	v_lshl_add_u64 v[78:79], v[212:213], 0, s[58:59]
	s_add_i32 s58, s45, s66
	s_mov_b32 m0, s58
	s_nop 0
	global_load_lds_dwordx4 v[78:79], off
	s_and_b64 vcc, exec, s[42:43]
	s_cbranch_vccnz .LBB0_1334
	s_lshl_b64 s[54:55], s[54:55], 11
	s_add_i32 s45, s45, s70
	v_lshl_add_u64 v[78:79], v[214:215], 0, s[54:55]
	s_mov_b32 m0, s45
	s_nop 0
	global_load_lds_dwordx4 v[78:79], off
